# speedup vs baseline: 1.1144x; 1.0050x over previous
.LBB0_7:
	s_or_b64 exec, exec, s[4:5]
	s_mov_b32 s34, 0x60441c00
	v_writelane_b32 v20, s34, 0
	s_mov_b32 s34, 0x53371d01
	v_writelane_b32 v20, s34, 1
	s_mov_b32 s34, 0x62461e02
	v_writelane_b32 v20, s34, 2
	s_mov_b32 s34, 0x6f471f03
	v_writelane_b32 v20, s34, 3
	s_mov_b32 s34, 0x78522a0e
	v_writelane_b32 v20, s34, 4
	s_mov_b32 s34, 0x61452b0f
	v_writelane_b32 v20, s34, 5
	s_mov_b32 s34, 0x6e543810
	v_writelane_b32 v20, s34, 6
	s_mov_b32 s34, 0x78553911
	v_writelane_b32 v20, s34, 7
	s_mov_b32 s34, 0x70482c12
	v_writelane_b32 v20, s34, 8
	s_mov_b32 s34, 0x71573b13
	v_writelane_b32 v20, s34, 9
	s_mov_b32 s34, 0x78643c14
	v_writelane_b32 v20, s34, 10
	s_mov_b32 s34, 0x734b2f15
	v_writelane_b32 v20, s34, 11
	s_mov_b32 s34, 0x563a2004
	v_writelane_b32 v20, s34, 12
	s_mov_b32 s34, 0x63492d05
	v_writelane_b32 v20, s34, 13
	s_mov_b32 s34, 0x724a2e06
	v_writelane_b32 v20, s34, 14
	s_mov_b32 s34, 0x653d2107
	v_writelane_b32 v20, s34, 15
	s_mov_b32 s34, 0x74583e22
	v_writelane_b32 v20, s34, 16
	s_mov_b32 s34, 0x78673f23
	v_writelane_b32 v20, s34, 17
	s_mov_b32 s34, 0x765a3216
	v_writelane_b32 v20, s34, 18
	s_mov_b32 s34, 0x775b4125
	v_writelane_b32 v20, s34, 19
	s_mov_b32 s34, 0x664c3008
	v_writelane_b32 v20, s34, 20
	s_mov_b32 s34, 0x75593109
	v_writelane_b32 v20, s34, 21
	s_mov_b32 s34, 0x6840240a
	v_writelane_b32 v20, s34, 22
	s_mov_b32 s34, 0x694d3317
	v_writelane_b32 v20, s34, 23
	s_mov_b32 s34, 0x785c3418
	v_writelane_b32 v20, s34, 24
	s_mov_b32 s34, 0x6b4f270b
	v_writelane_b32 v20, s34, 25
	s_mov_b32 s34, 0x5e42280c
	v_writelane_b32 v20, s34, 26
	s_mov_b32 s34, 0x6d51290d
	v_writelane_b32 v20, s34, 27
	s_mov_b32 s34, 0x786a4e26
	v_writelane_b32 v20, s34, 28
	s_mov_b32 s34, 0x785d3519
	v_writelane_b32 v20, s34, 29
	s_mov_b32 s34, 0x6c50361a
	v_writelane_b32 v20, s34, 30
	s_mov_b32 s34, 0x785f431b
	v_writelane_b32 v20, s34, 31
	s_mov_b32 s34, 0x54381c00
	v_writelane_b32 v22, s34, 0
	s_mov_b32 s34, 0x8c70
	v_writelane_b32 v23, s34, 0
	s_mov_b32 s34, 0x55391d01
	v_writelane_b32 v22, s34, 1
	s_mov_b32 s34, 0x8d71
	v_writelane_b32 v23, s34, 1
	s_mov_b32 s34, 0x563a1e02
	v_writelane_b32 v22, s34, 2
	s_mov_b32 s34, 0x8e72
	v_writelane_b32 v23, s34, 2
	s_mov_b32 s34, 0x573b1f03
	v_writelane_b32 v22, s34, 3
	s_mov_b32 s34, 0xa873
	v_writelane_b32 v23, s34, 3
	s_mov_b32 s34, 0x583c2004
	v_writelane_b32 v22, s34, 4
	s_mov_b32 s34, 0xa874
	v_writelane_b32 v23, s34, 4
	s_mov_b32 s34, 0x593d2105
	v_writelane_b32 v22, s34, 5
	s_mov_b32 s34, 0xa88f
	v_writelane_b32 v23, s34, 5
	s_mov_b32 s34, 0x5a3e2206
	v_writelane_b32 v22, s34, 6
	s_mov_b32 s34, 0xa890
	v_writelane_b32 v23, s34, 6
	s_mov_b32 s34, 0x753f2307
	v_writelane_b32 v22, s34, 7
	s_mov_b32 s34, 0xa891
	v_writelane_b32 v23, s34, 7
	s_mov_b32 s34, 0x76402408
	v_writelane_b32 v22, s34, 8
	s_mov_b32 s34, 0xa892
	v_writelane_b32 v23, s34, 8
	s_mov_b32 s34, 0x775b2509
	v_writelane_b32 v22, s34, 9
	s_mov_b32 s34, 0xa893
	v_writelane_b32 v23, s34, 9
	s_mov_b32 s34, 0x785c260a
	v_writelane_b32 v22, s34, 10
	s_mov_b32 s34, 0xa894
	v_writelane_b32 v23, s34, 10
	s_mov_b32 s34, 0x795d410b
	v_writelane_b32 v22, s34, 11
	s_mov_b32 s34, 0xa895
	v_writelane_b32 v23, s34, 11
	s_mov_b32 s34, 0x7a5e420c
	v_writelane_b32 v22, s34, 12
	s_mov_b32 s34, 0xa896
	v_writelane_b32 v23, s34, 12
	s_mov_b32 s34, 0x7b5f4327
	v_writelane_b32 v22, s34, 13
	s_mov_b32 s34, 0xa897
	v_writelane_b32 v23, s34, 13
	s_mov_b32 s34, 0x7c604428
	v_writelane_b32 v22, s34, 14
	s_mov_b32 s34, 0xa898
	v_writelane_b32 v23, s34, 14
	s_mov_b32 s34, 0x6145290d
	v_writelane_b32 v22, s34, 15
	s_mov_b32 s34, 0x997d
	v_writelane_b32 v23, s34, 15
	s_mov_b32 s34, 0x62462a0e
	v_writelane_b32 v22, s34, 16
	s_mov_b32 s34, 0x9a7e
	v_writelane_b32 v23, s34, 16
	s_mov_b32 s34, 0x63472b0f
	v_writelane_b32 v22, s34, 17
	s_mov_b32 s34, 0x9b7f
	v_writelane_b32 v23, s34, 17
	s_mov_b32 s34, 0x64482c10
	v_writelane_b32 v22, s34, 18
	s_mov_b32 s34, 0xa880
	v_writelane_b32 v23, s34, 18
	s_mov_b32 s34, 0x65492d11
	v_writelane_b32 v22, s34, 19
	s_mov_b32 s34, 0xa881
	v_writelane_b32 v23, s34, 19
	s_mov_b32 s34, 0x664a2e12
	v_writelane_b32 v22, s34, 20
	s_mov_b32 s34, 0xa89c
	v_writelane_b32 v23, s34, 20
	s_mov_b32 s34, 0x674b2f13
	v_writelane_b32 v22, s34, 21
	s_mov_b32 s34, 0xa89d
	v_writelane_b32 v23, s34, 21
	s_mov_b32 s34, 0x824c3014
	v_writelane_b32 v22, s34, 22
	s_mov_b32 s34, 0xa89e
	v_writelane_b32 v23, s34, 22
	s_mov_b32 s34, 0x834d3115
	v_writelane_b32 v22, s34, 23
	s_mov_b32 s34, 0xa89f
	v_writelane_b32 v23, s34, 23
	s_mov_b32 s34, 0x84683216
	v_writelane_b32 v22, s34, 24
	s_mov_b32 s34, 0xa8a0
	v_writelane_b32 v23, s34, 24
	s_mov_b32 s34, 0x85693317
	v_writelane_b32 v22, s34, 25
	s_mov_b32 s34, 0xa8a1
	v_writelane_b32 v23, s34, 25
	s_mov_b32 s34, 0x866a4e18
	v_writelane_b32 v22, s34, 26
	s_mov_b32 s34, 0xa8a2
	v_writelane_b32 v23, s34, 26
	s_mov_b32 s34, 0x876b4f19
	v_writelane_b32 v22, s34, 27
	s_mov_b32 s34, 0xa8a3
	v_writelane_b32 v23, s34, 27
	s_mov_b32 s34, 0x886c5034
	v_writelane_b32 v22, s34, 28
	s_mov_b32 s34, 0xa8a4
	v_writelane_b32 v23, s34, 28
	s_mov_b32 s34, 0x896d5135
	v_writelane_b32 v22, s34, 29
	s_mov_b32 s34, 0xa8a5
	v_writelane_b32 v23, s34, 29
	s_mov_b32 s34, 0x6e52361a
	v_writelane_b32 v22, s34, 30
	s_mov_b32 s34, 0xa68a
	v_writelane_b32 v23, s34, 30
	s_mov_b32 s34, 0x6f53371b
	v_writelane_b32 v22, s34, 31
	s_mov_b32 s34, 0xa78b
	v_writelane_b32 v23, s34, 31
	s_add_u32 s32, s20, s30
	s_addc_u32 s33, s21, 0
	v_lshlrev_b32_e32 v21, 2, v0
	v_add_u32_e32 v21, 0x21000, v21
	v_cmp_gt_u32_e32 vcc, 32, v0
	s_and_saveexec_b64 s[4:5], vcc
	global_store_dword v21, v20, s[32:33]
	global_store_dword v21, v22, s[32:33] offset:128
	global_store_dword v21, v23, s[32:33] offset:256
	s_or_b64 exec, exec, s[4:5]
	s_mov_b64 s[4:5], 0

_Z6k_mainPKfPKDv8_DF16_S0_S3_S0_S0_S0_S0_S0_S0_S0_S0_S0_S3_S0_S0_S0_S0_S0_S0_S0_S0_S0_S0_S0_S0_S0_Pf:
	s_load_dwordx4 s[60:63], s[0:1], 0xd0
	s_load_dwordx8 s[12:19], s[0:1], 0xb0
	s_load_dwordx8 s[36:43], s[0:1], 0x90
	s_load_dwordx8 s[44:51], s[0:1], 0x70
	s_load_dwordx2 s[10:11], s[0:1], 0x60
	s_load_dwordx8 s[24:31], s[0:1], 0x40
	s_load_dwordx2 s[20:21], s[0:1], 0x0
	s_load_dwordx8 s[52:59], s[0:1], 0x20
	s_load_dwordx4 s[84:87], s[0:1], 0x8
	s_load_dwordx2 s[90:91], s[0:1], 0x18
	s_movk_i32 s6, 0xe0
	v_mov_b32_e32 v1, 0xffffff1f
	v_cmp_lt_u32_e64 s[6:7], s6, v0
	s_movk_i32 s4, 0xe1
	s_movk_i32 s8, 0x1c2
	v_cndmask_b32_e64 v1, 0, v1, s[6:7]
	v_readfirstlane_b32 s3, v0
	v_cmp_gt_u32_e64 s[4:5], s4, v0
	v_add_u32_e32 v8, v1, v0
	v_cmp_gt_u32_e64 s[8:9], s8, v0
	s_and_b32 s88, s2, 7
	s_mul_i32 s88, s88, 0x30000
	s_waitcnt lgkmcnt(0)
	s_add_u32 s84, s84, s88
	s_addc_u32 s85, s85, 0
	s_add_u32 s86, s86, s88
	s_addc_u32 s87, s87, 0
	v_and_b32_e32 v30, 63, v0
	v_lshlrev_b32_e32 v30, 4, v30
	v_mov_b32_e32 v31, 0
	v_lshl_add_u64 v[32:33], s[84:85], 0, v[30:31]
	v_add_co_u32_e32 v32, vcc, 0x1000, v32
	v_bfe_u32 v34, v0, 5, 1
	v_lshlrev_b32_e32 v34, 2, v34
	v_addc_co_u32_e32 v33, vcc, 0, v33, vcc
	global_load_dwordx4 v[86:89], v30, s[84:85]
	global_load_dwordx4 v[62:65], v30, s[84:85] offset:1024
	global_load_dwordx4 v[58:61], v30, s[84:85] offset:2048
	global_load_dwordx4 v[54:57], v30, s[84:85] offset:3072
	global_load_dwordx4 v[50:53], v[32:33], off
	global_load_dword v46, v34, s[86:87]
	global_load_dword v47, v34, s[86:87] offset:8
	global_load_dword v48, v34, s[86:87] offset:16
	global_load_dword v49, v34, s[86:87] offset:24
	s_add_u32 s90, s90, s88
	s_addc_u32 s91, s91, 0
	v_and_b32_e32 v117, 31, v0
	v_lshlrev_b32_e32 v117, 2, v117
	v_add_u32_e32 v117, 0x21000, v117
	global_load_dword v113, v117, s[90:91] offset:256
	global_load_dword v112, v117, s[90:91] offset:128
	global_load_dword v117, v117, s[90:91]
	s_and_saveexec_b64 s[22:23], s[8:9]
	s_cbranch_execz .LBB1_4
	s_mul_i32 s34, s2, 0x6978
	s_mul_hi_i32 s33, s2, 0x6978
	s_waitcnt lgkmcnt(0)
	s_add_u32 s34, s20, s34
	v_mov_b32_e32 v1, 0x3840
	s_addc_u32 s35, s21, s33
	v_cndmask_b32_e64 v2, 0, v1, s[6:7]
	v_mov_b32_e32 v3, 0
	v_lshl_add_u64 v[4:5], s[34:35], 0, v[2:3]
	v_mov_b32_e32 v9, v3
	v_lshl_add_u64 v[4:5], v[8:9], 2, v[4:5]
	s_movk_i32 s33, 0x1000
	v_add_co_u32_e32 v16, vcc, s33, v4
	v_mov_b32_e32 v7, v3
	s_nop 0
	v_addc_co_u32_e32 v17, vcc, 0, v5, vcc
	global_load_dword v1, v[4:5], off
	global_load_dword v2, v[4:5], off offset:900
	global_load_dword v6, v[4:5], off offset:1800
	global_load_dword v9, v[4:5], off offset:2700
	global_load_dword v10, v[4:5], off offset:3600
	global_load_dword v11, v[16:17], off offset:404
	global_load_dword v12, v[16:17], off offset:1304
	global_load_dword v13, v[16:17], off offset:2204
	v_add_co_u32_e32 v18, vcc, 0x2000, v4
	s_nop 1
	v_addc_co_u32_e32 v19, vcc, 0, v5, vcc
	global_load_dword v14, v[16:17], off offset:3104
	s_nop 0
	global_load_dword v16, v[16:17], off offset:4004
	s_nop 0
	global_load_dword v17, v[18:19], off offset:808
	global_load_dword v28, v[18:19], off offset:1708
	global_load_dword v27, v[18:19], off offset:2608
	global_load_dword v29, v[18:19], off offset:3508
	s_and_saveexec_b64 s[34:35], s[4:5]
	s_cbranch_execz .LBB1_3
	v_add_co_u32_e32 v4, vcc, 0x3000, v4
	s_nop 1
	v_addc_co_u32_e32 v5, vcc, 0, v5, vcc
	global_load_dword v3, v[4:5], off offset:312
	s_nop 0
	global_load_dword v4, v[4:5], off offset:1212
	s_waitcnt vmcnt(1)
	v_cvt_f16_f32_e32 v3, v3
	s_waitcnt vmcnt(0)
	v_cvt_f16_f32_e32 v7, v4

.LBB1_15:
	s_or_b64 exec, exec, s[12:13]
	v_and_b32_e32 v114, 31, v0
	s_mul_i32 s9, s67, 0x60
	s_cmp_lg_u32 s67, 0
	s_cselect_b64 s[74:75], -1, 0
	v_alignbit_b32 v126, v113, v112, 24
	v_cndmask_b32_e64 v126, v112, v126, s[74:75]
	v_bfe_u32 v91, v126, 0, 8
	v_mul_lo_u16_e32 v15, 0x4f, v91
	s_lshl_b32 s7, s66, 3
	v_lshrrev_b16_e32 v15, 9, v15
	s_or_b32 s8, s7, 0xb600
	v_and_b32_e32 v15, 62, v15
	v_add_u32_e32 v15, v91, v15
	s_movk_i32 s6, 0x48
	v_mov_b32_e32 v99, s8
	v_mad_u32_u24 v42, v15, s6, v99
	v_mad_u32_u24 v43, v115, s6, v42
	s_waitcnt lgkmcnt(0)
	s_barrier
	ds_read_b64 v[34:35], v43
	ds_read_b64 v[36:37], v43 offset:8
	ds_read_b64 v[38:39], v43 offset:1080
	ds_read_b64 v[40:41], v43 offset:1088
	v_mov_b32_e32 v2, v46
	v_mov_b32_e32 v3, v46
	v_mov_b32_e32 v4, v46
	v_mov_b32_e32 v5, v46
	v_mov_b32_e32 v6, v47
	v_mov_b32_e32 v7, v47
	v_mov_b32_e32 v8, v47
	v_mov_b32_e32 v9, v47
	v_mov_b32_e32 v10, v48
	v_mov_b32_e32 v11, v48
	v_mov_b32_e32 v12, v48
	v_mov_b32_e32 v13, v48
	v_mov_b32_e32 v14, v49
	v_mov_b32_e32 v15, v49
	v_mov_b32_e32 v16, v49
	v_mov_b32_e32 v17, v49
	s_movk_i32 s8, 0x438
	s_add_i32 s12, s9, 32
	s_waitcnt lgkmcnt(2)
	v_mfma_f32_32x32x16_f16 v[18:33], v[86:89], v[34:37], v[2:17]
	v_add_u32_e32 v34, 0x8b8, v43
	ds_read_b64 v[36:37], v34 offset:8
	ds_read_b64 v[34:35], v34
	v_and_or_b32 v107, v0, 32, s7
	s_movk_i32 s7, 0x110
	v_mad_u32_u24 v91, v91, s7, v107
	s_add_i32 s9, s9, 64
	s_lshr_b32 s42, s3, 6
	s_waitcnt lgkmcnt(2)
	v_mfma_f32_32x32x16_f16 v[18:33], v[62:65], v[38:41], v[18:33]
	v_mad_u32_u24 v38, v115, s8, v42
	ds_read_b64 v[40:41], v38 offset:152
	ds_read_b64 v[38:39], v38 offset:144
	s_cmpk_lt_u32 s3, 0x100
	s_cselect_b64 s[30:31], -1, 0
	s_add_i32 s13, s69, 0x600
	s_add_i32 s14, s69, 0x700
	v_lshlrev_b32_e32 v116, 4, v115
	s_waitcnt lgkmcnt(2)
	v_mfma_f32_32x32x16_f16 v[18:33], v[58:61], v[34:37], v[18:33]
	v_add_u32_e32 v34, 0x870, v43
	ds_read_b64 v[36:37], v34 offset:8
	ds_read_b64 v[34:35], v34
	s_movk_i32 s15, 0x1070
	s_movk_i32 s16, 0x1ba0
	s_movk_i32 s17, 0x1c20
	s_waitcnt lgkmcnt(2)
	v_mfma_f32_32x32x16_f16 v[18:33], v[54:57], v[38:41], v[18:33]
	v_bfe_u32 v101, v126, 8, 8
	v_mul_lo_u16_e32 v38, 0x4f, v101
	v_lshrrev_b16_e32 v38, 9, v38
	v_and_b32_e32 v38, 62, v38
	v_add_u32_e32 v38, v101, v38
	v_mad_u32_u24 v97, v38, s6, v99
	v_mad_u32_u24 v106, v115, s6, v97
	ds_read_b64 v[92:93], v106
	ds_read_b64 v[94:95], v106 offset:8
	v_add_u32_e32 v96, 0x8b8, v106
	ds_read_b64 v[102:103], v96
	ds_read_b64 v[104:105], v96 offset:8
	s_waitcnt lgkmcnt(4)
	v_mfma_f32_32x32x16_f16 v[18:33], v[50:53], v[34:37], v[18:33]
	s_add_i32 s12, s69, 0x500
	s_addk_i32 s69, 0x800
	s_cmpk_gt_u32 s3, 0xff
	s_cselect_b64 vcc, -1, 0
	s_waitcnt lgkmcnt(2)
	v_mfma_f32_32x32x16_f16 v[34:49], v[86:89], v[92:95], v[2:17]
	ds_read_b64 v[92:93], v106 offset:1080
	ds_read_b64 v[94:95], v106 offset:1088
	s_nop 4
	v_cvt_pk_f16_f32 v18, v18, v19
	v_pk_max_f16 v96, v18, 0
	v_mad_u32_u24 v18, v115, s8, v97
	v_cvt_pk_f16_f32 v22, v22, v23
	v_add_u32_e32 v23, 0x870, v106
	v_cvt_pk_f16_f32 v30, v30, v31
	s_waitcnt lgkmcnt(0)
	v_mfma_f32_32x32x16_f16 v[34:49], v[62:65], v[92:95], v[34:49]
	v_cvt_pk_f16_f32 v92, v20, v21
	ds_read_b64 v[20:21], v18 offset:152
	ds_read_b64 v[18:19], v18 offset:144
	v_pk_max_f16 v97, v92, 0
	ds_read_b64 v[92:93], v23
	ds_read_b64 v[94:95], v23 offset:8
	v_cvt_pk_f16_f32 v31, v32, v33
	v_mfma_f32_32x32x16_f16 v[34:49], v[58:61], v[102:105], v[34:49]
	v_or_b32_e32 v102, 64, v114
	s_waitcnt lgkmcnt(2)
	v_mfma_f32_32x32x16_f16 v[34:49], v[54:57], v[18:21], v[34:49]
	v_cvt_pk_f16_f32 v19, v24, v25
	v_pk_max_f16 v18, v22, 0
	v_pk_max_f16 v19, v19, 0
	ds_write2_b64 v91, v[96:97], v[18:19] offset1:8
	v_cvt_pk_f16_f32 v18, v26, v27
	v_pk_max_f16 v26, v18, 0
	v_cvt_pk_f16_f32 v22, v28, v29
	v_bfe_u32 v28, v126, 16, 8
	v_mul_lo_u16_e32 v18, 0x4f, v28
	v_lshrrev_b16_e32 v18, 9, v18
	v_and_b32_e32 v18, 62, v18
	v_add_u32_e32 v18, v28, v18
	v_mad_u32_u24 v29, v18, s6, v99
	s_waitcnt lgkmcnt(1)
	v_mfma_f32_32x32x16_f16 v[34:49], v[50:53], v[92:95], v[34:49]
	v_add_u32_e32 v94, s68, v100
	v_add_u32_e32 v94, s69, v94
	v_mov_b32_e32 v95, 0
	v_lshl_add_u64 v[94:95], v[94:95], 4, s[22:23]
	global_load_dwordx4 v[94:97], v[94:95], off
	v_mad_u32_u24 v92, v115, s6, v29
	ds_read_b64 v[18:19], v92
	ds_read_b64 v[20:21], v92 offset:8
	v_pk_max_f16 v27, v22, 0
	ds_read_b64 v[22:23], v92 offset:1080
	ds_read_b64 v[24:25], v92 offset:1088
	v_or_b32_e32 v99, 32, v114
	s_nop 6
	v_cvt_pk_f16_f32 v32, v40, v41
	s_waitcnt lgkmcnt(2)
	v_mfma_f32_32x32x16_f16 v[2:17], v[86:89], v[18:21], v[2:17]
	v_pk_max_f16 v18, v30, 0
	v_pk_max_f16 v19, v31, 0
	ds_write2_b64 v91, v[26:27], v[18:19] offset0:16 offset1:24
	v_cvt_pk_f16_f32 v18, v34, v35
	v_cvt_pk_f16_f32 v19, v36, v37
	v_pk_max_f16 v26, v18, 0
	v_add_u32_e32 v18, 0x8b8, v92
	s_waitcnt lgkmcnt(1)
	v_mfma_f32_32x32x16_f16 v[2:17], v[62:65], v[22:25], v[2:17]
	v_pk_max_f16 v27, v19, 0
	ds_read_b64 v[20:21], v18 offset:8
	ds_read_b64 v[18:19], v18
	v_mad_u32_u24 v22, v115, s8, v29
	ds_read_b64 v[24:25], v22 offset:152
	ds_read_b64 v[22:23], v22 offset:144
	v_cvt_pk_f16_f32 v31, v38, v39
	v_mad_u32_u24 v30, v101, s7, v107
	s_and_b64 s[8:9], vcc, exec
	s_waitcnt lgkmcnt(2)
	v_mfma_f32_32x32x16_f16 v[2:17], v[58:61], v[18:21], v[2:17]
	v_pk_max_f16 v18, v31, 0
	v_pk_max_f16 v19, v32, 0
	ds_write2_b64 v30, v[26:27], v[18:19] offset1:8
	v_cvt_pk_f16_f32 v18, v42, v43
	v_cvt_pk_f16_f32 v19, v44, v45
	v_pk_max_f16 v26, v18, 0
	v_add_u32_e32 v18, 0x870, v92
	s_waitcnt lgkmcnt(1)
	v_mfma_f32_32x32x16_f16 v[2:17], v[54:57], v[22:25], v[2:17]
	v_pk_max_f16 v27, v19, 0
	ds_read_b64 v[20:21], v18 offset:8
	ds_read_b64 v[18:19], v18
	v_cvt_pk_f16_f32 v22, v46, v47
	v_cvt_pk_f16_f32 v23, v48, v49
	v_pk_max_f16 v22, v22, 0
	v_pk_max_f16 v23, v23, 0
	ds_write2_b64 v30, v[26:27], v[22:23] offset0:16 offset1:24
	s_waitcnt lgkmcnt(1)
	v_mfma_f32_32x32x16_f16 v[2:17], v[50:53], v[18:21], v[2:17]
	v_mad_u32_u24 v18, v28, s7, v107
	v_lshl_or_b32 v42, s66, 5, v116
	s_cselect_b32 s8, 0xf60, 0
	s_movk_i32 s9, 0xff0
	s_cselect_b32 s9, s9, 0x80
	s_cselect_b32 s15, s15, 0x110
	s_cselect_b32 s16, s16, 0x190
	s_nop 4
	v_cvt_pk_f16_f32 v2, v2, v3
	v_cvt_pk_f16_f32 v3, v4, v5
	v_cvt_pk_f16_f32 v4, v6, v7
	v_cvt_pk_f16_f32 v5, v8, v9
	v_pk_max_f16 v2, v2, 0
	v_pk_max_f16 v3, v3, 0
	v_pk_max_f16 v4, v4, 0
	v_pk_max_f16 v5, v5, 0
	ds_write2_b64 v18, v[2:3], v[4:5] offset1:8
	v_cvt_pk_f16_f32 v2, v10, v11
	v_cvt_pk_f16_f32 v3, v12, v13
	v_cvt_pk_f16_f32 v4, v14, v15
	v_cvt_pk_f16_f32 v5, v16, v17
	v_pk_max_f16 v2, v2, 0
	v_pk_max_f16 v3, v3, 0
	v_pk_max_f16 v4, v4, 0
	v_pk_max_f16 v5, v5, 0
	ds_write2_b64 v18, v[2:3], v[4:5] offset0:16 offset1:24
	s_waitcnt vmcnt(0)
	v_bfe_u32 v2, v117, 0, 8
	v_mul_u32_u24_e32 v3, 0xbb, v2
	v_lshrrev_b32_e32 v3, 11, v3
	v_lshl_add_u32 v103, v3, 1, v2
	v_bfe_u32 v2, v117, 8, 8
	v_mul_u32_u24_e32 v3, 0xbb, v2
	v_lshrrev_b32_e32 v3, 11, v3
	v_lshl_add_u32 v106, v3, 1, v2
	v_mad_u32_u24 v90, v103, s7, v42
	v_mad_u32_u24 v91, v106, s7, v42
	v_add_u32_e32 v2, s8, v90
	v_add_u32_e32 v6, s8, v91
	s_waitcnt lgkmcnt(0)
	s_barrier
	ds_read_b128 v[2:5], v2
	ds_read_b128 v[6:9], v6
	s_waitcnt lgkmcnt(1)
	v_mfma_f32_32x32x16_f16 v[18:33], v[82:85], v[2:5], 0
	v_add_u32_e32 v34, s9, v90
	v_add_u32_e32 v38, s9, v91
	ds_read_b128 v[34:37], v34
	ds_read_b128 v[38:41], v38
	s_cselect_b32 s17, s17, 0x220
	v_or_b32_e32 v101, 0x60, v114
	s_waitcnt lgkmcnt(2)
	v_mfma_f32_32x32x16_f16 v[2:17], v[82:85], v[6:9], 0
	s_waitcnt lgkmcnt(1)
	v_mfma_f32_32x32x16_f16 v[18:33], v[74:77], v[34:37], v[18:33]
	v_add_u32_e32 v34, s15, v90
	ds_read_b128 v[34:37], v34
	s_waitcnt lgkmcnt(1)
	v_mfma_f32_32x32x16_f16 v[2:17], v[74:77], v[38:41], v[2:17]
	v_add_u32_e32 v38, s15, v91
	ds_read_b128 v[38:41], v38
	s_waitcnt lgkmcnt(1)
	v_mfma_f32_32x32x16_f16 v[18:33], v[78:81], v[34:37], v[18:33]
	v_add_u32_e32 v34, s16, v90
	ds_read_b128 v[34:37], v34
	s_waitcnt lgkmcnt(1)
	v_mfma_f32_32x32x16_f16 v[2:17], v[78:81], v[38:41], v[2:17]
	v_add_u32_e32 v38, s16, v91
	ds_read_b128 v[38:41], v38
	s_waitcnt lgkmcnt(1)
	v_mfma_f32_32x32x16_f16 v[18:33], v[70:73], v[34:37], v[18:33]
	v_bfe_u32 v43, v117, 16, 8
	v_mul_u32_u24_e32 v34, 0xbb, v43
	v_lshrrev_b32_e32 v104, 11, v34
	v_add_u32_e32 v34, s17, v90
	ds_read_b128 v[34:37], v34
	v_lshl_add_u32 v104, v104, 1, v43
	v_mad_u32_u24 v92, v104, s7, v42
	s_waitcnt lgkmcnt(1)
	v_mfma_f32_32x32x16_f16 v[2:17], v[70:73], v[38:41], v[2:17]
	v_add_u32_e32 v38, s17, v91
	ds_read_b128 v[38:41], v38
	s_waitcnt lgkmcnt(1)
	v_mfma_f32_32x32x16_f16 v[18:33], v[66:69], v[34:37], v[18:33]
	v_bfe_u32 v34, v117, 24, 8
	v_mul_u32_u24_e32 v35, 0xbb, v34
	v_lshrrev_b32_e32 v35, 11, v35
	v_lshl_add_u32 v105, v35, 1, v34
	v_mad_u32_u24 v93, v105, s7, v42
	s_waitcnt lgkmcnt(0)
	v_mfma_f32_32x32x16_f16 v[2:17], v[66:69], v[38:41], v[2:17]
	v_add_u32_e32 v34, s8, v92
	v_add_u32_e32 v38, s8, v93
	ds_read_b128 v[34:37], v34
	ds_read_b128 v[38:41], v38
	v_add_u32_e32 v86, s9, v93
	s_waitcnt lgkmcnt(1)
	v_mfma_f32_32x32x16_f16 v[50:65], v[82:85], v[34:37], 0
	ds_read_b128 v[86:89], v86
	s_waitcnt lgkmcnt(1)
	v_mfma_f32_32x32x16_f16 v[34:49], v[82:85], v[38:41], 0
	v_add_u32_e32 v82, s9, v92
	ds_read_b128 v[82:85], v82
	s_waitcnt lgkmcnt(0)
	v_mfma_f32_32x32x16_f16 v[50:65], v[74:77], v[82:85], v[50:65]
	v_add_u32_e32 v82, s15, v93
	ds_read_b128 v[82:85], v82
	v_mfma_f32_32x32x16_f16 v[34:49], v[74:77], v[86:89], v[34:49]
	v_add_u32_e32 v74, s15, v92
	ds_read_b128 v[74:77], v74
	s_waitcnt lgkmcnt(0)
	v_mfma_f32_32x32x16_f16 v[50:65], v[78:81], v[74:77], v[50:65]
	v_add_u32_e32 v74, s16, v92
	ds_read_b128 v[74:77], v74
	v_mfma_f32_32x32x16_f16 v[34:49], v[78:81], v[82:85], v[34:49]
	v_add_u32_e32 v78, s16, v93
	ds_read_b128 v[78:81], v78
	s_waitcnt lgkmcnt(1)
	v_mfma_f32_32x32x16_f16 v[50:65], v[70:73], v[74:77], v[50:65]
	v_add_u32_e32 v74, s17, v93
	ds_read_b128 v[74:77], v74
	s_waitcnt lgkmcnt(1)
	v_mfma_f32_32x32x16_f16 v[34:49], v[70:73], v[78:81], v[34:49]
	v_add_u32_e32 v70, s17, v92
	ds_read_b128 v[70:73], v70
	s_waitcnt lgkmcnt(0)
	v_mfma_f32_32x32x16_f16 v[50:65], v[66:69], v[70:73], v[50:65]
	v_mfma_f32_32x32x16_f16 v[34:49], v[66:69], v[74:77], v[34:49]
	s_movk_i32 s7, 0x1cb0
	s_cselect_b32 s7, s7, 0x2a0
	v_add_u32_e32 v74, s7, v90
	ds_read_b128 v[74:77], v74
	v_add_u32_e32 v78, s7, v91
	ds_read_b128 v[78:81], v78
	s_movk_i32 s12, 0x1d30
	s_cselect_b32 s12, s12, 0xdd0
	s_movk_i32 s8, 0x1dc0
	s_cselect_b32 s8, s8, 0xe50
	s_movk_i32 s9, 0x1e40
	s_cselect_b32 s9, s9, 0xee0
	s_waitcnt vmcnt(0) lgkmcnt(1)
	v_mfma_f32_32x32x16_f16 v[18:33], v[108:111], v[74:77], v[18:33]
	v_add_u32_e32 v82, s12, v91
	ds_read_b128 v[82:85], v82
	s_waitcnt lgkmcnt(1)
	v_mfma_f32_32x32x16_f16 v[2:17], v[108:111], v[78:81], v[2:17]
	v_add_u32_e32 v78, s12, v90
	ds_read_b128 v[78:81], v78
	s_waitcnt lgkmcnt(0)
	v_mfma_f32_32x32x16_f16 v[18:33], v[118:121], v[78:81], v[18:33]
	v_add_u32_e32 v86, s8, v91
	ds_read_b128 v[86:89], v86
	v_mfma_f32_32x32x16_f16 v[2:17], v[118:121], v[82:85], v[2:17]
	v_add_u32_e32 v82, s8, v90
	ds_read_b128 v[82:85], v82
	s_waitcnt lgkmcnt(0)
	v_mfma_f32_32x32x16_f16 v[18:33], v[122:125], v[82:85], v[18:33]
	v_add_u32_e32 v82, s9, v90
	ds_read_b128 v[82:85], v82
	v_mfma_f32_32x32x16_f16 v[2:17], v[122:125], v[86:89], v[2:17]
	v_add_u32_e32 v86, s9, v91
	ds_read_b128 v[86:89], v86
	s_waitcnt lgkmcnt(1)
	v_mfma_f32_32x32x16_f16 v[18:33], v[94:97], v[82:85], v[18:33]
	s_waitcnt lgkmcnt(0)
	v_mfma_f32_32x32x16_f16 v[2:17], v[94:97], v[86:89], v[2:17]
	v_add_u32_e32 v82, s7, v92
	v_add_u32_e32 v86, s7, v93
	ds_read_b128 v[82:85], v82
	ds_read_b128 v[86:89], v86
	s_waitcnt lgkmcnt(1)
	v_mfma_f32_32x32x16_f16 v[50:65], v[108:111], v[82:85], v[50:65]
	v_add_u32_e32 v82, s12, v93
	ds_read_b128 v[82:85], v82
	s_waitcnt lgkmcnt(1)
	v_mfma_f32_32x32x16_f16 v[34:49], v[108:111], v[86:89], v[34:49]
	v_add_u32_e32 v66, s12, v92
	ds_read_b128 v[66:69], v66
	s_waitcnt lgkmcnt(0)
	v_mfma_f32_32x32x16_f16 v[50:65], v[118:121], v[66:69], v[50:65]
	v_add_u32_e32 v66, s8, v92
	ds_read_b128 v[66:69], v66
	v_mfma_f32_32x32x16_f16 v[34:49], v[118:121], v[82:85], v[34:49]
	v_add_u32_e32 v70, s8, v93
	ds_read_b128 v[70:73], v70
	s_waitcnt lgkmcnt(1)
	v_mfma_f32_32x32x16_f16 v[50:65], v[122:125], v[66:69], v[50:65]
	v_add_u32_e32 v66, s9, v92
	ds_read_b128 v[66:69], v66
	s_waitcnt lgkmcnt(1)
	v_mfma_f32_32x32x16_f16 v[34:49], v[122:125], v[70:73], v[34:49]
	v_add_u32_e32 v70, s9, v93
	ds_read_b128 v[70:73], v70
	s_waitcnt lgkmcnt(1)
	v_mfma_f32_32x32x16_f16 v[50:65], v[94:97], v[66:69], v[50:65]
	s_waitcnt lgkmcnt(0)
	v_mfma_f32_32x32x16_f16 v[34:49], v[94:97], v[70:73], v[34:49]
	s_cmpk_gt_u32 s3, 0x17f
	s_barrier
	s_cbranch_scc1 .LBB1_17
	s_mul_hi_u32 s7, s42, 0x55555556
	s_mul_i32 s7, s7, 3
	s_sub_i32 s7, s42, s7
	s_lshl_b32 s7, s7, 3
	s_add_i32 s8, s7, 0xb600
	s_cmpk_gt_u32 s3, 0xbf
	s_cselect_b64 s[74:75], -1, 0
	s_movk_i32 s12, 0x438
	s_movk_i32 s13, 0xd0
	v_alignbit_b32 v99, v113, v112, 24
	v_cndmask_b32_e64 v99, v112, v99, s[74:75]
	v_add_u32_e32 v122, 0xf550, v98
	ds_read_b128 v[82:85], v98 offset:62800
	ds_read_b128 v[86:89], v98 offset:63824
	ds_read_b128 v[90:93], v98 offset:64848
	ds_read_b128 v[94:97], v122 offset:3072
	ds_read_b128 v[118:121], v122 offset:4096
	ds_read_b32 v107, v122 offset:5120
	ds_read_b32 v112, v122 offset:5124
	ds_read_b32 v113, v122 offset:5128
	ds_read_b32 v117, v122 offset:5132
	v_bfe_u32 v101, v99, 0, 8
	v_mul_lo_u16_e32 v102, 0x4f, v101
	v_lshrrev_b16_e32 v102, 9, v102
	v_and_b32_e32 v102, 62, v102
	v_add_u32_e32 v102, v101, v102
	v_mov_b32_e32 v123, s8
	v_mad_u32_u24 v102, v102, s6, v123
	v_mad_u32_u24 v123, v115, s6, v102
	v_mad_u32_u24 v102, v115, s12, v102
	v_mad_u32_u24 v122, v115, 24, s7
	v_mad_u32_u24 v101, v101, s13, v122
	ds_read_b64 v[108:109], v123 offset:32
	ds_read_b64 v[110:111], v123 offset:40
	ds_read_b64 v[124:125], v123 offset:1112
	ds_read_b64 v[126:127], v123 offset:1120
	v_add_u32_e32 v122, 0x8d8, v123
	s_waitcnt lgkmcnt(2)
	v_mfma_f32_32x32x16_f16 v[66:81], v[82:85], v[108:111], 0
	ds_read_b64 v[108:109], v122
	ds_read_b64 v[110:111], v122 offset:8
	v_add_u32_e32 v122, 0x890, v123
	s_waitcnt lgkmcnt(2)
	v_mfma_f32_32x32x16_f16 v[66:81], v[86:89], v[124:127], v[66:81]
	ds_read_b64 v[124:125], v102 offset:176
	ds_read_b64 v[126:127], v102 offset:184
	s_waitcnt lgkmcnt(2)
	v_mfma_f32_32x32x16_f16 v[66:81], v[90:93], v[108:111], v[66:81]
	ds_read_b64 v[108:109], v122
	ds_read_b64 v[110:111], v122 offset:8
	s_waitcnt lgkmcnt(2)
	v_mfma_f32_32x32x16_f16 v[66:81], v[94:97], v[124:127], v[66:81]
	s_waitcnt lgkmcnt(0)
	v_mfma_f32_32x32x16_f16 v[66:81], v[118:121], v[108:111], v[66:81]
	v_bfe_u32 v124, v99, 8, 8
	v_mul_lo_u16_e32 v126, 0x4f, v124
	v_lshrrev_b16_e32 v126, 9, v126
	v_and_b32_e32 v126, 62, v126
	v_add_u32_e32 v126, v124, v126
	v_mov_b32_e32 v123, s8
	v_mad_u32_u24 v126, v126, s6, v123
	v_mad_u32_u24 v123, v115, s6, v126
	v_mad_u32_u24 v102, v115, s12, v126
	v_mad_u32_u24 v122, v115, 24, s7
	v_mad_u32_u24 v125, v124, s13, v122
	ds_read_b64 v[108:109], v123 offset:32
	ds_read_b64 v[110:111], v123 offset:40
	v_add_f32_e32 v66, v107, v66
	v_add_f32_e32 v67, v107, v67
	v_add_f32_e32 v68, v107, v68
	v_add_f32_e32 v69, v107, v69
	v_add_f32_e32 v70, v112, v70
	v_add_f32_e32 v71, v112, v71
	v_add_f32_e32 v72, v112, v72
	v_add_f32_e32 v73, v112, v73
	v_add_f32_e32 v74, v113, v74
	v_add_f32_e32 v75, v113, v75
	v_add_f32_e32 v76, v113, v76
	v_add_f32_e32 v77, v113, v77
	v_add_f32_e32 v78, v117, v78
	v_add_f32_e32 v79, v117, v79
	v_add_f32_e32 v80, v117, v80
	v_add_f32_e32 v81, v117, v81
	v_cvt_pk_f16_f32 v66, v66, v67
	v_cvt_pk_f16_f32 v67, v68, v69
	v_cvt_pk_f16_f32 v68, v70, v71
	v_cvt_pk_f16_f32 v69, v72, v73
	v_cvt_pk_f16_f32 v70, v74, v75
	v_cvt_pk_f16_f32 v71, v76, v77
	v_cvt_pk_f16_f32 v72, v78, v79
	v_cvt_pk_f16_f32 v73, v80, v81
	v_pk_max_f16 v66, v66, 0
	v_pk_max_f16 v67, v67, 0
	v_pk_max_f16 v68, v68, 0
	v_pk_max_f16 v69, v69, 0
	v_pk_max_f16 v70, v70, 0
	v_pk_max_f16 v71, v71, 0
	v_pk_max_f16 v72, v72, 0
	v_pk_max_f16 v73, v73, 0
	ds_write2_b64 v101, v[66:67], v[68:69] offset1:6
	ds_write2_b64 v101, v[70:71], v[72:73] offset0:12 offset1:18
	v_mov_b32_e32 v101, v125
	ds_read_b64 v[124:125], v123 offset:1112
	ds_read_b64 v[126:127], v123 offset:1120
	v_add_u32_e32 v122, 0x8d8, v123
	s_waitcnt lgkmcnt(2)
	v_mfma_f32_32x32x16_f16 v[66:81], v[82:85], v[108:111], 0
	ds_read_b64 v[108:109], v122
	ds_read_b64 v[110:111], v122 offset:8
	v_add_u32_e32 v122, 0x890, v123
	s_waitcnt lgkmcnt(2)
	v_mfma_f32_32x32x16_f16 v[66:81], v[86:89], v[124:127], v[66:81]
	ds_read_b64 v[124:125], v102 offset:176
	ds_read_b64 v[126:127], v102 offset:184
	s_waitcnt lgkmcnt(2)
	v_mfma_f32_32x32x16_f16 v[66:81], v[90:93], v[108:111], v[66:81]
	ds_read_b64 v[108:109], v122
	ds_read_b64 v[110:111], v122 offset:8
	s_waitcnt lgkmcnt(2)
	v_mfma_f32_32x32x16_f16 v[66:81], v[94:97], v[124:127], v[66:81]
	s_waitcnt lgkmcnt(0)
	v_mfma_f32_32x32x16_f16 v[66:81], v[118:121], v[108:111], v[66:81]
	v_bfe_u32 v124, v99, 16, 8
	v_mul_lo_u16_e32 v126, 0x4f, v124
	v_lshrrev_b16_e32 v126, 9, v126
	v_and_b32_e32 v126, 62, v126
	v_add_u32_e32 v126, v124, v126
	v_mov_b32_e32 v123, s8
	v_mad_u32_u24 v126, v126, s6, v123
	v_mad_u32_u24 v123, v115, s6, v126
	v_mad_u32_u24 v102, v115, s12, v126
	v_mad_u32_u24 v122, v115, 24, s7
	v_mad_u32_u24 v125, v124, s13, v122
	ds_read_b64 v[108:109], v123 offset:32
	ds_read_b64 v[110:111], v123 offset:40
	v_add_f32_e32 v66, v107, v66
	v_add_f32_e32 v67, v107, v67
	v_add_f32_e32 v68, v107, v68
	v_add_f32_e32 v69, v107, v69
	v_add_f32_e32 v70, v112, v70
	v_add_f32_e32 v71, v112, v71
	v_add_f32_e32 v72, v112, v72
	v_add_f32_e32 v73, v112, v73
	v_add_f32_e32 v74, v113, v74
	v_add_f32_e32 v75, v113, v75
	v_add_f32_e32 v76, v113, v76
	v_add_f32_e32 v77, v113, v77
	v_add_f32_e32 v78, v117, v78
	v_add_f32_e32 v79, v117, v79
	v_add_f32_e32 v80, v117, v80
	v_add_f32_e32 v81, v117, v81
	v_cvt_pk_f16_f32 v66, v66, v67
	v_cvt_pk_f16_f32 v67, v68, v69
	v_cvt_pk_f16_f32 v68, v70, v71
	v_cvt_pk_f16_f32 v69, v72, v73
	v_cvt_pk_f16_f32 v70, v74, v75
	v_cvt_pk_f16_f32 v71, v76, v77
	v_cvt_pk_f16_f32 v72, v78, v79
	v_cvt_pk_f16_f32 v73, v80, v81
	v_pk_max_f16 v66, v66, 0
	v_pk_max_f16 v67, v67, 0
	v_pk_max_f16 v68, v68, 0
	v_pk_max_f16 v69, v69, 0
	v_pk_max_f16 v70, v70, 0
	v_pk_max_f16 v71, v71, 0
	v_pk_max_f16 v72, v72, 0
	v_pk_max_f16 v73, v73, 0
	ds_write2_b64 v101, v[66:67], v[68:69] offset1:6
	ds_write2_b64 v101, v[70:71], v[72:73] offset0:12 offset1:18
	v_mov_b32_e32 v101, v125
	ds_read_b64 v[124:125], v123 offset:1112
	ds_read_b64 v[126:127], v123 offset:1120
	v_add_u32_e32 v122, 0x8d8, v123
	s_waitcnt lgkmcnt(2)
	v_mfma_f32_32x32x16_f16 v[66:81], v[82:85], v[108:111], 0
	ds_read_b64 v[108:109], v122
	ds_read_b64 v[110:111], v122 offset:8
	v_add_u32_e32 v122, 0x890, v123
	s_waitcnt lgkmcnt(2)
	v_mfma_f32_32x32x16_f16 v[66:81], v[86:89], v[124:127], v[66:81]
	ds_read_b64 v[124:125], v102 offset:176
	ds_read_b64 v[126:127], v102 offset:184
	s_waitcnt lgkmcnt(2)
	v_mfma_f32_32x32x16_f16 v[66:81], v[90:93], v[108:111], v[66:81]
	ds_read_b64 v[108:109], v122
	ds_read_b64 v[110:111], v122 offset:8
	s_waitcnt lgkmcnt(2)
	v_mfma_f32_32x32x16_f16 v[66:81], v[94:97], v[124:127], v[66:81]
	s_waitcnt lgkmcnt(0)
	v_mfma_f32_32x32x16_f16 v[66:81], v[118:121], v[108:111], v[66:81]
	v_or_b32_e32 v99, 32, v114
	v_or_b32_e32 v102, 64, v114
	s_nop 9
	v_add_f32_e32 v66, v107, v66
	v_add_f32_e32 v67, v107, v67
	v_add_f32_e32 v68, v107, v68
	v_add_f32_e32 v69, v107, v69
	v_add_f32_e32 v70, v112, v70
	v_add_f32_e32 v71, v112, v71
	v_add_f32_e32 v72, v112, v72
	v_add_f32_e32 v73, v112, v73
	v_add_f32_e32 v74, v113, v74
	v_add_f32_e32 v75, v113, v75
	v_add_f32_e32 v76, v113, v76
	v_add_f32_e32 v77, v113, v77
	v_add_f32_e32 v78, v117, v78
	v_add_f32_e32 v79, v117, v79
	v_add_f32_e32 v80, v117, v80
	v_add_f32_e32 v81, v117, v81
	v_cvt_pk_f16_f32 v66, v66, v67
	v_cvt_pk_f16_f32 v67, v68, v69
	v_cvt_pk_f16_f32 v68, v70, v71
	v_cvt_pk_f16_f32 v69, v72, v73
	v_cvt_pk_f16_f32 v70, v74, v75
	v_cvt_pk_f16_f32 v71, v76, v77
	v_cvt_pk_f16_f32 v72, v78, v79
	v_cvt_pk_f16_f32 v73, v80, v81
	v_pk_max_f16 v66, v66, 0
	v_pk_max_f16 v67, v67, 0
	v_pk_max_f16 v68, v68, 0
	v_pk_max_f16 v69, v69, 0
	v_pk_max_f16 v70, v70, 0
	v_pk_max_f16 v71, v71, 0
	v_pk_max_f16 v72, v72, 0
	v_pk_max_f16 v73, v73, 0
	ds_write2_b64 v101, v[66:67], v[68:69] offset1:6
	ds_write2_b64 v101, v[70:71], v[72:73] offset0:12 offset1:18
	v_or_b32_e32 v101, 0x60, v114
